# nomov
# speedup vs baseline: 1.0011x; 1.0011x over previous
.LBB1_12:
	s_and_b32 s12, s19, 1
	s_lshr_b32 s13, s19, 1
	s_add_i32 s16, s19, 1
	v_lshl_add_u32 v231, s13, 3, v221
	s_cmp_lg_u32 s19, 3
	s_cselect_b32 s17, s16, 3
	s_waitcnt lgkmcnt(2)
	v_lshlrev_b32_e32 v2, 7, v231
	s_lshl_b32 s14, s12, 6
	v_or3_b32 v160, v2, s14, v220
	s_waitcnt lgkmcnt(0)
	v_mov_b32_e32 v1, v220
	v_lshl_add_u64 v[2:3], v[160:161], 2, s[6:7]
	global_load_dword v232, v[2:3], off
	s_lshl_b32 s14, s17, 2
	s_and_b32 s14, s14, 24
	s_lshl_b32 s13, s13, 9
	v_lshrrev_b32_e32 v3, 5, v1
	s_cmp_eq_u32 s12, 0
	v_add_u32_e32 v2, s14, v221
	v_lshlrev_b32_e32 v206, 4, v3
	s_cselect_b64 s[14:15], -1, 0
	s_cmp_eq_u32 s12, 1
	v_add3_u32 v149, v228, s13, v206
	s_cselect_b64 s[12:13], -1, 0
	s_lshl_b32 s17, s17, 6
	s_and_b32 s17, s17, 64
	v_lshl_or_b32 v2, v2, 7, s17
	v_lshl_add_u32 v234, v1, 4, 0
	v_and_or_b32 v1, v1, 31, v2
	v_mul_lo_u32 v2, v1, 27
	v_add_u32_e32 v233, 0xc000, v234
	v_mad_u64_u32 v[204:205], s[20:21], v3, 14, v[2:3]
	v_add_u32_e32 v202, 13, v2
	s_waitcnt vmcnt(3)
	v_mul_f32_e32 v1, 0.15915494, v222
	v_cos_f32_e32 v2, v1
	v_sin_f32_e32 v1, v1
	v_add_f32_e32 v2, v2, v2
	v_cndmask_b32_e64 v3, v2, v1, s[0:1]
	v_mul_f32_e32 v1, v1, v2
	v_fma_f32 v2, v2, v2, -2.0
	v_cndmask_b32_e64 v4, v2, v1, s[0:1]
	v_mul_f32_e32 v207, v1, v2
	v_fma_f32 v208, v2, v2, -2.0
	v_mul_f32_e32 v2, 0.15915494, v182
	v_cvt_pk_fp8_f32 v131, v225, v3
	v_cos_f32_e32 v3, v2
	v_sin_f32_e32 v2, v2
	v_cndmask_b32_e64 v1, v208, v207, s[0:1]
	v_cvt_pk_fp8_f32 v131, v4, v1 op_sel:[0,0,1]
	v_add_f32_e32 v1, v3, v3
	v_cvt_pk_f16_f32 v1, v2, v1
	v_cvt_pk_fp8_f32 v128, v182, v0
	v_cvt_scalef32_pk_fp8_f16 v132, v1, 1.0
	v_pk_fma_f16 v1, v1, v1, -2.0 op_sel:[1,0,1] op_sel_hi:[1,1,0]
	v_mul_f32_e32 v0, 0.15915494, v0
	v_cvt_scalef32_pk_fp8_f16 v132, v1, 1.0 op_sel:[0,0,1]
	v_pk_fma_f16 v1, v1, v1, -2.0 op_sel:[0,1,1] op_sel_hi:[1,1,0]
	v_cos_f32_e32 v2, v0
	v_cvt_scalef32_pk_fp8_f16 v133, v1, 1.0
	v_pk_fma_f16 v1, v1, v1, -2.0 op_sel:[0,1,1] op_sel_hi:[1,1,0]
	v_sin_f32_e32 v0, v0
	v_cvt_scalef32_pk_fp8_f16 v133, v1, 1.0 op_sel:[0,0,1]
	v_pk_fma_f16 v1, v1, v1, -2.0 op_sel:[0,1,1] op_sel_hi:[1,1,0]
	s_nop 0
	v_cvt_scalef32_pk_fp8_f16 v134, v1, 1.0
	v_pk_fma_f16 v1, v1, v1, -2.0 op_sel:[0,1,1] op_sel_hi:[1,1,0]
	s_nop 0
	v_cvt_scalef32_pk_fp8_f16 v134, v1, 1.0 op_sel:[0,0,1]
	v_add_f32_e32 v1, v2, v2
	v_cvt_pk_f16_f32 v0, v0, v1
	v_cvt_scalef32_pk_fp8_f16 v135, v0, 1.0
	v_pk_fma_f16 v24, v0, v0, -2.0 op_sel:[1,0,1] op_sel_hi:[1,1,0]
	s_waitcnt vmcnt(2)
	v_mul_f32_e32 v0, 0.15915494, v224
	v_cos_f32_e32 v1, v0
	v_sin_f32_e32 v0, v0
	v_add_f32_e32 v1, v1, v1
	v_cndmask_b32_e64 v2, v1, v0, s[0:1]
	v_mul_f32_e32 v0, v0, v1
	v_fma_f32 v1, v1, v1, -2.0
	v_cndmask_b32_e64 v3, v1, v0, s[0:1]
	v_mul_f32_e32 v209, v0, v1
	v_fma_f32 v210, v1, v1, -2.0
	v_mul_f32_e32 v1, 0.15915494, v190
	s_waitcnt vmcnt(1)
	v_cvt_pk_fp8_f32 v19, v223, v2
	v_cos_f32_e32 v2, v1
	v_sin_f32_e32 v1, v1
	v_cndmask_b32_e64 v0, v210, v209, s[0:1]
	v_cvt_pk_fp8_f32 v19, v3, v0 op_sel:[0,0,1]
	v_add_f32_e32 v0, v2, v2
	v_cvt_pk_f16_f32 v0, v1, v0
	v_cvt_scalef32_pk_fp8_f16 v20, v0, 1.0
	v_pk_fma_f16 v0, v0, v0, -2.0 op_sel:[1,0,1] op_sel_hi:[1,1,0]
	v_mul_f32_e32 v1, 0.15915494, v191
	v_cvt_scalef32_pk_fp8_f16 v135, v24, 1.0 op_sel:[0,0,1]
	v_cvt_scalef32_pk_fp8_f16 v20, v0, 1.0 op_sel:[0,0,1]
	v_pk_fma_f16 v0, v0, v0, -2.0 op_sel:[0,1,1] op_sel_hi:[1,1,0]
	v_cos_f32_e32 v2, v1
	v_pk_fma_f16 v24, v24, v24, -2.0 op_sel:[0,1,1] op_sel_hi:[1,1,0]
	v_cvt_scalef32_pk_fp8_f16 v21, v0, 1.0
	v_pk_fma_f16 v0, v0, v0, -2.0 op_sel:[0,1,1] op_sel_hi:[1,1,0]
	v_sin_f32_e32 v1, v1
	v_pk_fma_f16 v35, v24, v24, -2.0 op_sel:[0,1,1] op_sel_hi:[1,1,0]
	v_cvt_pk_fp8_f32 v128, v25, v185 op_sel:[0,0,1]
	v_cvt_scalef32_pk_fp8_f16 v21, v0, 1.0 op_sel:[0,0,1]
	v_pk_fma_f16 v0, v0, v0, -2.0 op_sel:[0,1,1] op_sel_hi:[1,1,0]
	v_pk_fma_f16 v36, v35, v35, -2.0 op_sel:[0,1,1] op_sel_hi:[1,1,0]
	v_mul_f32_e32 v25, 0.15915494, v25
	v_cvt_pk_fp8_f32 v129, v198, v162
	v_cvt_pk_fp8_f32 v130, v178, v200
	v_cvt_pk_fp8_f32 v16, v190, v191
	v_cvt_pk_fp8_f32 v17, v194, v195
	v_cvt_pk_fp8_f32 v18, v186, v187
	v_cvt_scalef32_pk_fp8_f16 v22, v0, 1.0
	v_pk_fma_f16 v0, v0, v0, -2.0 op_sel:[0,1,1] op_sel_hi:[1,1,0]
	v_pk_fma_f16 v37, v36, v36, -2.0 op_sel:[0,1,1] op_sel_hi:[1,1,0]
	v_cvt_scalef32_pk_fp8_f16 v137, v36, 1.0
	v_cos_f32_e32 v36, v25
	v_cvt_scalef32_pk_fp8_f16 v22, v0, 1.0 op_sel:[0,0,1]
	v_add_f32_e32 v0, v2, v2
	v_sin_f32_e32 v25, v25
	v_cvt_pk_f16_f32 v0, v1, v0
	v_mov_b32_e32 v160, v204
	v_cvt_scalef32_pk_fp8_f16 v23, v0, 1.0
	v_pk_fma_f16 v34, v0, v0, -2.0 op_sel:[1,0,1] op_sel_hi:[1,1,0]
	ds_read_b128 v[26:29], v234
	ds_read_b128 v[30:33], v234 offset:1024
	ds_read_b128 v[8:11], v234 offset:2048
	ds_read_b128 v[12:15], v234 offset:3072
	ds_read_b128 v[0:3], v234 offset:4096
	ds_read_b128 v[4:7], v234 offset:5120
	ds_read_b128 v[152:155], v234 offset:6144
	ds_read_b128 v[156:159], v234 offset:7168
	ds_read_b128 v[96:99], v149
	ds_read_b128 v[100:103], v149 offset:32
	ds_read_b128 v[104:107], v149 offset:64
	ds_read_b128 v[108:111], v149 offset:96
	v_cvt_pk_fp8_f32 v129, v163, v201 op_sel:[0,0,1]
	v_cvt_pk_fp8_f32 v130, v179, v181 op_sel:[0,0,1]
	v_cvt_pk_fp8_f32 v16, v192, v193 op_sel:[0,0,1]
	v_cvt_pk_fp8_f32 v17, v196, v197 op_sel:[0,0,1]
	v_cvt_pk_fp8_f32 v18, v188, v189 op_sel:[0,0,1]
	v_cvt_scalef32_pk_fp8_f16 v136, v24, 1.0
	v_add_f32_e32 v24, v36, v36
	v_cvt_pk_f16_f32 v24, v25, v24
	v_pk_fma_f16 v25, v24, v24, -2.0 op_sel:[1,0,1] op_sel_hi:[1,1,0]
	v_cvt_scalef32_pk_fp8_f16 v138, v24, 1.0
	v_cvt_scalef32_pk_fp8_f16 v23, v34, 1.0 op_sel:[0,0,1]
	v_cvt_scalef32_pk_fp8_f16 v136, v35, 1.0 op_sel:[0,0,1]
	v_pk_fma_f16 v35, v25, v25, -2.0 op_sel:[0,1,1] op_sel_hi:[1,1,0]
	v_cvt_scalef32_pk_fp8_f16 v138, v25, 1.0 op_sel:[0,0,1]
	v_mul_f32_e32 v25, 0.15915494, v185
	s_waitcnt lgkmcnt(0)
	v_mfma_scale_f32_32x32x64_f8f6f4 v[112:127], v[26:33], v[16:23], v[96:111], v227, v226 op_sel_hi:[0,0,0]
	v_cvt_scalef32_pk_fp8_f16 v139, v35, 1.0
	v_pk_fma_f16 v35, v35, v35, -2.0 op_sel:[0,1,1] op_sel_hi:[1,1,0]
	s_nop 0
	v_pk_fma_f16 v24, v35, v35, -2.0 op_sel:[0,1,1] op_sel_hi:[1,1,0]
	ds_read_b128 v[64:67], v149 offset:128
	ds_read_b128 v[68:71], v149 offset:160
	ds_read_b128 v[72:75], v149 offset:192
	ds_read_b128 v[76:79], v149 offset:224
	v_cvt_scalef32_pk_fp8_f16 v140, v24, 1.0
	v_pk_fma_f16 v24, v24, v24, -2.0 op_sel:[0,1,1] op_sel_hi:[1,1,0]
	v_cvt_scalef32_pk_fp8_f16 v137, v37, 1.0 op_sel:[0,0,1]
	v_cvt_scalef32_pk_fp8_f16 v140, v24, 1.0 op_sel:[0,0,1]
	v_cvt_scalef32_pk_fp8_f16 v139, v35, 1.0 op_sel:[0,0,1]
	v_mfma_scale_f32_32x32x64_f8f6f4 v[96:111], v[26:33], v[128:135], v[96:111], v227, v226 op_sel_hi:[0,0,0]
	v_cos_f32_e32 v26, v25
	v_sin_f32_e32 v25, v25
	v_mul_f32_e32 v30, 0.15915494, v192
	v_mul_f32_e32 v31, 0.15915494, v193
	v_add_f32_e32 v24, v26, v26
	v_cvt_pk_f16_f32 v24, v25, v24
	v_cvt_scalef32_pk_fp8_f16 v141, v24, 1.0
	v_pk_fma_f16 v24, v24, v24, -2.0 op_sel:[1,0,1] op_sel_hi:[1,1,0]
	s_nop 0
	v_cvt_scalef32_pk_fp8_f16 v141, v24, 1.0 op_sel:[0,0,1]
	v_pk_fma_f16 v26, v24, v24, -2.0 op_sel:[0,1,1] op_sel_hi:[1,1,0]
	v_lshl_add_u64 v[24:25], v[160:161], 2, s[4:5]
	v_pk_fma_f16 v27, v26, v26, -2.0 op_sel:[0,1,1] op_sel_hi:[1,1,0]
	s_nop 0
	v_pk_fma_f16 v28, v27, v27, -2.0 op_sel:[0,1,1] op_sel_hi:[1,1,0]
	s_waitcnt lgkmcnt(0)
	v_mfma_scale_f32_32x32x64_f8f6f4 v[80:95], v[8:15], v[16:23], v[64:79], v227, v226 op_sel_hi:[0,0,0]
	global_load_dwordx4 v[182:185], v[24:25], off
	global_load_dwordx4 v[190:193], v[24:25], off offset:3456
	v_cos_f32_e32 v25, v31
	v_pk_fma_f16 v29, v28, v28, -2.0 op_sel:[0,1,1] op_sel_hi:[1,1,0]
	v_cvt_scalef32_pk_fp8_f16 v143, v28, 1.0
	v_cvt_scalef32_pk_fp8_f16 v142, v26, 1.0
	v_cvt_scalef32_pk_fp8_f16 v143, v29, 1.0 op_sel:[0,0,1]
	v_cvt_scalef32_pk_fp8_f16 v142, v27, 1.0 op_sel:[0,0,1]
	v_add_f32_e32 v150, v25, v25
	v_mfma_scale_f32_32x32x64_f8f6f4 v[64:79], v[8:15], v[128:135], v[64:79], v227, v226 op_sel_hi:[0,0,0]
	v_pk_fma_f16 v8, v34, v34, -2.0 op_sel:[0,1,1] op_sel_hi:[1,1,0]
	ds_read_b128 v[32:35], v149 offset:256
	ds_read_b128 v[36:39], v149 offset:288
	ds_read_b128 v[40:43], v149 offset:320
	ds_read_b128 v[44:47], v149 offset:352
	v_pk_fma_f16 v9, v8, v8, -2.0 op_sel:[0,1,1] op_sel_hi:[1,1,0]
	v_cvt_scalef32_pk_fp8_f16 v144, v8, 1.0
	v_pk_fma_f16 v10, v9, v9, -2.0 op_sel:[0,1,1] op_sel_hi:[1,1,0]
	v_cvt_scalef32_pk_fp8_f16 v144, v9, 1.0 op_sel:[0,0,1]
	v_pk_fma_f16 v11, v10, v10, -2.0 op_sel:[0,1,1] op_sel_hi:[1,1,0]
	v_cvt_scalef32_pk_fp8_f16 v145, v10, 1.0
	v_cos_f32_e32 v10, v30
	v_cvt_scalef32_pk_fp8_f16 v145, v11, 1.0 op_sel:[0,0,1]
	v_sin_f32_e32 v11, v30
	v_add_f32_e32 v8, v10, v10
	v_cvt_pk_f16_f32 v8, v11, v8
	v_pk_fma_f16 v9, v8, v8, -2.0 op_sel:[1,0,1] op_sel_hi:[1,1,0]
	v_cvt_scalef32_pk_fp8_f16 v146, v8, 1.0
	v_pk_fma_f16 v10, v9, v9, -2.0 op_sel:[0,1,1] op_sel_hi:[1,1,0]
	s_waitcnt lgkmcnt(0)
	v_mfma_scale_f32_32x32x64_f8f6f4 v[48:63], v[0:7], v[16:23], v[32:47], v227, v226 op_sel_hi:[0,0,0]
	v_cvt_scalef32_pk_fp8_f16 v147, v10, 1.0
	v_pk_fma_f16 v10, v10, v10, -2.0 op_sel:[0,1,1] op_sel_hi:[1,1,0]
	v_cvt_scalef32_pk_fp8_f16 v146, v9, 1.0 op_sel:[0,0,1]
	v_cvt_scalef32_pk_fp8_f16 v147, v10, 1.0 op_sel:[0,0,1]
	v_pk_fma_f16 v24, v10, v10, -2.0 op_sel:[0,1,1] op_sel_hi:[1,1,0]
	s_nop 0
	v_cvt_scalef32_pk_fp8_f16 v148, v24, 1.0
	v_pk_fma_f16 v24, v24, v24, -2.0 op_sel:[0,1,1] op_sel_hi:[1,1,0]
	s_nop 0
	v_cvt_scalef32_pk_fp8_f16 v148, v24, 1.0 op_sel:[0,0,1]
	v_mfma_scale_f32_32x32x64_f8f6f4 v[32:47], v[0:7], v[128:135], v[32:47], v227, v226 op_sel_hi:[0,0,0]
	ds_read_b128 v[0:3], v149 offset:384
	ds_read_b128 v[4:7], v149 offset:416
	ds_read_b128 v[8:11], v149 offset:448
	ds_read_b128 v[12:15], v149 offset:480
	v_sin_f32_e32 v149, v31
	s_nop 0
	v_cvt_pk_f16_f32 v150, v149, v150
	v_cvt_scalef32_pk_fp8_f16 v149, v150, 1.0
	v_pk_fma_f16 v150, v150, v150, -2.0 op_sel:[1,0,1] op_sel_hi:[1,1,0]
	s_nop 0
	v_pk_fma_f16 v160, v150, v150, -2.0 op_sel:[0,1,1] op_sel_hi:[1,1,0]
	v_cvt_scalef32_pk_fp8_f16 v149, v150, 1.0 op_sel:[0,0,1]
	v_pk_fma_f16 v164, v160, v160, -2.0 op_sel:[0,1,1] op_sel_hi:[1,1,0]
	s_nop 0
	v_pk_fma_f16 v150, v164, v164, -2.0 op_sel:[0,1,1] op_sel_hi:[1,1,0]
	s_waitcnt lgkmcnt(0)
	v_mfma_scale_f32_32x32x64_f8f6f4 v[16:31], v[152:159], v[16:23], v[0:15], v227, v226 op_sel_hi:[0,0,0]
	v_pk_fma_f16 v165, v150, v150, -2.0 op_sel:[0,1,1] op_sel_hi:[1,1,0]
	v_cvt_scalef32_pk_fp8_f16 v151, v150, 1.0
	v_cvt_scalef32_pk_fp8_f16 v150, v160, 1.0
	v_cvt_scalef32_pk_fp8_f16 v151, v165, 1.0 op_sel:[0,0,1]
	v_cvt_scalef32_pk_fp8_f16 v150, v164, 1.0 op_sel:[0,0,1]
	v_mfma_scale_f32_32x32x64_f8f6f4 v[0:15], v[152:159], v[128:135], v[0:15], v227, v226 op_sel_hi:[0,0,0]
	v_mul_f32_e32 v128, 0.15915494, v198
	v_cos_f32_e32 v129, v128
	v_sin_f32_e32 v128, v128
	v_mul_f32_e32 v133, 0.15915494, v162
	v_cos_f32_e32 v134, v133
	v_add_f32_e32 v129, v129, v129
	v_cvt_pk_f16_f32 v130, v128, v129
	v_pk_fma_f16 v131, v130, v130, -2.0 op_sel:[1,0,1] op_sel_hi:[1,1,0]
	v_sin_f32_e32 v133, v133
	v_pk_fma_f16 v128, v131, v131, -2.0 op_sel:[0,1,1] op_sel_hi:[1,1,0]
	s_nop 0
	v_pk_fma_f16 v132, v128, v128, -2.0 op_sel:[0,1,1] op_sel_hi:[1,1,0]
	v_cvt_scalef32_pk_fp8_f16 v129, v128, 1.0
	v_cvt_scalef32_pk_fp8_f16 v128, v130, 1.0
	v_add_f32_e32 v130, v134, v134
	v_cvt_scalef32_pk_fp8_f16 v128, v131, 1.0 op_sel:[0,0,1]
	v_cvt_pk_f16_f32 v130, v133, v130
	v_cvt_scalef32_pk_fp8_f16 v129, v132, 1.0 op_sel:[0,0,1]
	v_cvt_scalef32_pk_fp8_f16 v131, v130, 1.0
	v_pk_fma_f16 v133, v130, v130, -2.0 op_sel:[1,0,1] op_sel_hi:[1,1,0]
	v_pk_fma_f16 v132, v132, v132, -2.0 op_sel:[0,1,1] op_sel_hi:[1,1,0]
	ds_read_b128 v[152:155], v234 offset:8192
	ds_read_b128 v[156:159], v234 offset:9216
	ds_read_b128 v[164:167], v234 offset:10240
	ds_read_b128 v[168:171], v234 offset:11264
	ds_read_b128 v[236:239], v234 offset:12288
	ds_read_b128 v[240:243], v234 offset:13312
	v_cvt_scalef32_pk_fp8_f16 v130, v132, 1.0
	v_pk_fma_f16 v132, v132, v132, -2.0 op_sel:[0,1,1] op_sel_hi:[1,1,0]
	v_mul_f32_e32 v135, 0.15915494, v163
	s_waitcnt lgkmcnt(4)
	v_mfma_scale_f32_32x32x64_f8f6f4 v[96:111], v[152:159], v[136:143], v[96:111], v227, v226 op_sel_hi:[0,0,0]
	v_cvt_scalef32_pk_fp8_f16 v131, v133, 1.0 op_sel:[0,0,1]
	v_pk_fma_f16 v133, v133, v133, -2.0 op_sel:[0,1,1] op_sel_hi:[1,1,0]
	v_cvt_scalef32_pk_fp8_f16 v130, v132, 1.0 op_sel:[0,0,1]
	v_cvt_scalef32_pk_fp8_f16 v132, v133, 1.0
	v_pk_fma_f16 v133, v133, v133, -2.0 op_sel:[0,1,1] op_sel_hi:[1,1,0]
	ds_read_b128 v[244:247], v234 offset:14336
	ds_read_b128 v[248:251], v234 offset:15360
	v_pk_fma_f16 v134, v133, v133, -2.0 op_sel:[0,1,1] op_sel_hi:[1,1,0]
	v_cvt_scalef32_pk_fp8_f16 v132, v133, 1.0 op_sel:[0,0,1]
	v_cvt_scalef32_pk_fp8_f16 v133, v134, 1.0
	v_pk_fma_f16 v134, v134, v134, -2.0 op_sel:[0,1,1] op_sel_hi:[1,1,0]
	s_nop 0
	v_cvt_scalef32_pk_fp8_f16 v133, v134, 1.0 op_sel:[0,0,1]
	v_mfma_scale_f32_32x32x64_f8f6f4 v[112:127], v[152:159], v[144:151], v[112:127], v227, v226 op_sel_hi:[0,0,0]
	v_cos_f32_e32 v152, v135
	v_sin_f32_e32 v135, v135
	v_mul_f32_e32 v154, 0.15915494, v194
	v_cos_f32_e32 v155, v154
	v_add_f32_e32 v134, v152, v152
	v_cvt_pk_f16_f32 v152, v135, v134
	v_pk_fma_f16 v153, v152, v152, -2.0 op_sel:[1,0,1] op_sel_hi:[1,1,0]
	v_sin_f32_e32 v154, v154
	v_pk_fma_f16 v134, v153, v153, -2.0 op_sel:[0,1,1] op_sel_hi:[1,1,0]
	s_nop 0
	v_pk_fma_f16 v160, v134, v134, -2.0 op_sel:[0,1,1] op_sel_hi:[1,1,0]
	v_cvt_scalef32_pk_fp8_f16 v135, v134, 1.0
	v_cvt_scalef32_pk_fp8_f16 v134, v152, 1.0
	v_add_f32_e32 v152, v155, v155
	s_waitcnt lgkmcnt(4)
	v_mfma_scale_f32_32x32x64_f8f6f4 v[64:79], v[164:171], v[136:143], v[64:79], v227, v226 op_sel_hi:[0,0,0]
	v_mul_f32_e32 v157, 0.15915494, v195
	v_cvt_pk_f16_f32 v154, v154, v152
	v_cos_f32_e32 v158, v157
	v_pk_fma_f16 v155, v154, v154, -2.0 op_sel:[1,0,1] op_sel_hi:[1,1,0]
	v_sin_f32_e32 v157, v157
	v_pk_fma_f16 v152, v155, v155, -2.0 op_sel:[0,1,1] op_sel_hi:[1,1,0]
	v_cvt_scalef32_pk_fp8_f16 v134, v153, 1.0 op_sel:[0,0,1]
	v_pk_fma_f16 v156, v152, v152, -2.0 op_sel:[0,1,1] op_sel_hi:[1,1,0]
	v_cvt_scalef32_pk_fp8_f16 v153, v152, 1.0
	v_cvt_scalef32_pk_fp8_f16 v152, v154, 1.0
	v_add_f32_e32 v154, v158, v158
	v_mul_f32_e32 v159, 0.15915494, v196
	v_cvt_scalef32_pk_fp8_f16 v152, v155, 1.0 op_sel:[0,0,1]
	v_mfma_scale_f32_32x32x64_f8f6f4 v[80:95], v[164:171], v[144:151], v[80:95], v227, v226 op_sel_hi:[0,0,0]
	v_cvt_pk_f16_f32 v154, v157, v154
	v_cvt_scalef32_pk_fp8_f16 v153, v156, 1.0 op_sel:[0,0,1]
	v_cvt_scalef32_pk_fp8_f16 v155, v154, 1.0
	v_pk_fma_f16 v156, v156, v156, -2.0 op_sel:[0,1,1] op_sel_hi:[1,1,0]
	v_pk_fma_f16 v157, v154, v154, -2.0 op_sel:[1,0,1] op_sel_hi:[1,1,0]
	v_cvt_scalef32_pk_fp8_f16 v154, v156, 1.0
	v_pk_fma_f16 v156, v156, v156, -2.0 op_sel:[0,1,1] op_sel_hi:[1,1,0]
	v_cvt_scalef32_pk_fp8_f16 v155, v157, 1.0 op_sel:[0,0,1]
	v_pk_fma_f16 v157, v157, v157, -2.0 op_sel:[0,1,1] op_sel_hi:[1,1,0]
	v_cvt_scalef32_pk_fp8_f16 v154, v156, 1.0 op_sel:[0,0,1]
	v_cvt_scalef32_pk_fp8_f16 v156, v157, 1.0
	v_pk_fma_f16 v157, v157, v157, -2.0 op_sel:[0,1,1] op_sel_hi:[1,1,0]
	s_waitcnt lgkmcnt(0)
	v_mfma_scale_f32_32x32x64_f8f6f4 v[0:15], v[244:251], v[136:143], v[0:15], v227, v226 op_sel_hi:[0,0,0]
	v_cvt_scalef32_pk_fp8_f16 v156, v157, 1.0 op_sel:[0,0,1]
	v_pk_fma_f16 v158, v157, v157, -2.0 op_sel:[0,1,1] op_sel_hi:[1,1,0]
	v_cvt_scalef32_pk_fp8_f16 v135, v160, 1.0 op_sel:[0,0,1]
	v_cvt_scalef32_pk_fp8_f16 v157, v158, 1.0
	v_mfma_scale_f32_32x32x64_f8f6f4 v[32:47], v[236:243], v[136:143], v[32:47], v227, v226 op_sel_hi:[0,0,0]
	v_cos_f32_e32 v136, v159
	v_sin_f32_e32 v137, v159
	v_pk_fma_f16 v138, v158, v158, -2.0 op_sel:[0,1,1] op_sel_hi:[1,1,0]
	v_add_f32_e32 v136, v136, v136
	v_cvt_pk_f16_f32 v136, v137, v136
	v_pk_fma_f16 v137, v136, v136, -2.0 op_sel:[1,0,1] op_sel_hi:[1,1,0]
	v_cvt_scalef32_pk_fp8_f16 v157, v138, 1.0 op_sel:[0,0,1]
	v_pk_fma_f16 v138, v137, v137, -2.0 op_sel:[0,1,1] op_sel_hi:[1,1,0]
	s_nop 0
	v_pk_fma_f16 v180, v138, v138, -2.0 op_sel:[0,1,1] op_sel_hi:[1,1,0]
	v_cvt_scalef32_pk_fp8_f16 v159, v138, 1.0
	v_cvt_scalef32_pk_fp8_f16 v158, v136, 1.0
	v_cvt_scalef32_pk_fp8_f16 v159, v180, 1.0 op_sel:[0,0,1]
	v_cvt_scalef32_pk_fp8_f16 v158, v137, 1.0 op_sel:[0,0,1]
	v_mfma_scale_f32_32x32x64_f8f6f4 v[48:63], v[236:243], v[144:151], v[48:63], v227, v226 op_sel_hi:[0,0,0]
	v_mfma_scale_f32_32x32x64_f8f6f4 v[16:31], v[244:251], v[144:151], v[16:31], v227, v226 op_sel_hi:[0,0,0]
	ds_read_b128 v[140:143], v234 offset:16384
	ds_read_b128 v[144:147], v234 offset:17408
	ds_read_b128 v[236:239], v234 offset:18432
	ds_read_b128 v[240:243], v234 offset:19456
	ds_read_b128 v[170:173], v234 offset:20480
	ds_read_b128 v[174:177], v234 offset:21504
	s_waitcnt lgkmcnt(4)
	v_mfma_scale_f32_32x32x64_f8f6f4 v[96:111], v[140:147], v[128:135], v[96:111], v227, v226 op_sel_hi:[0,0,0]
	v_pk_fma_f16 v139, v160, v160, -2.0 op_sel:[0,1,1] op_sel_hi:[1,1,0]
	v_mov_b32_e32 v160, v204
	ds_read_b128 v[162:165], v234 offset:22528
	ds_read_b128 v[166:169], v234 offset:23552
	v_mul_f32_e32 v136, 0.15915494, v201
	v_cos_f32_e32 v137, v136
	v_sin_f32_e32 v136, v136
	v_mul_f32_e32 v150, 0.15915494, v186
	v_cos_f32_e32 v151, v150
	v_add_f32_e32 v137, v137, v137
	v_cvt_pk_f16_f32 v136, v136, v137
	v_pk_fma_f16 v138, v136, v136, -2.0 op_sel:[1,0,1] op_sel_hi:[1,1,0]
	v_cvt_scalef32_pk_fp8_f16 v137, v136, 1.0
	v_mfma_scale_f32_32x32x64_f8f6f4 v[112:127], v[140:147], v[152:159], v[112:127], v227, v226 op_sel_hi:[0,0,0]
	v_mul_f32_e32 v140, 0.15915494, v178
	v_cos_f32_e32 v141, v140
	v_sin_f32_e32 v140, v140
	v_mul_f32_e32 v143, 0.15915494, v200
	v_cos_f32_e32 v144, v143
	v_add_f32_e32 v141, v141, v141
	v_cvt_pk_f16_f32 v141, v140, v141
	v_sin_f32_e32 v143, v143
	v_cvt_scalef32_pk_fp8_f16 v140, v141, 1.0
	v_pk_fma_f16 v141, v141, v141, -2.0 op_sel:[1,0,1] op_sel_hi:[1,1,0]
	v_mul_f32_e32 v146, 0.15915494, v197
	v_pk_fma_f16 v142, v141, v141, -2.0 op_sel:[0,1,1] op_sel_hi:[1,1,0]
	v_cvt_scalef32_pk_fp8_f16 v140, v141, 1.0 op_sel:[0,0,1]
	v_cvt_scalef32_pk_fp8_f16 v141, v142, 1.0
	v_pk_fma_f16 v145, v142, v142, -2.0 op_sel:[0,1,1] op_sel_hi:[1,1,0]
	v_add_f32_e32 v142, v144, v144
	v_cvt_pk_f16_f32 v144, v143, v142
	v_lshl_add_u64 v[142:143], v[160:161], 2, s[4:5]
	global_load_dwordx4 v[198:201], v[142:143], off offset:16
	global_load_dwordx4 v[194:197], v[142:143], off offset:3472
	v_cvt_scalef32_pk_fp8_f16 v141, v145, 1.0 op_sel:[0,0,1]
	v_pk_fma_f16 v160, v144, v144, -2.0 op_sel:[1,0,1] op_sel_hi:[1,1,0]
	v_cvt_scalef32_pk_fp8_f16 v143, v144, 1.0
	v_pk_fma_f16 v144, v145, v145, -2.0 op_sel:[0,1,1] op_sel_hi:[1,1,0]
	v_cos_f32_e32 v145, v146
	v_sin_f32_e32 v146, v146
	v_pk_fma_f16 v148, v138, v138, -2.0 op_sel:[0,1,1] op_sel_hi:[1,1,0]
	v_cvt_scalef32_pk_fp8_f16 v136, v139, 1.0
	v_pk_fma_f16 v139, v139, v139, -2.0 op_sel:[0,1,1] op_sel_hi:[1,1,0]
	v_pk_fma_f16 v149, v148, v148, -2.0 op_sel:[0,1,1] op_sel_hi:[1,1,0]
	v_cvt_scalef32_pk_fp8_f16 v142, v144, 1.0
	v_pk_fma_f16 v144, v144, v144, -2.0 op_sel:[0,1,1] op_sel_hi:[1,1,0]
	v_cvt_scalef32_pk_fp8_f16 v137, v138, 1.0 op_sel:[0,0,1]
	v_cvt_scalef32_pk_fp8_f16 v136, v139, 1.0 op_sel:[0,0,1]
	v_pk_fma_f16 v138, v149, v149, -2.0 op_sel:[0,1,1] op_sel_hi:[1,1,0]
	v_cvt_scalef32_pk_fp8_f16 v142, v144, 1.0 op_sel:[0,0,1]
	v_add_f32_e32 v144, v145, v145
	v_cvt_scalef32_pk_fp8_f16 v139, v138, 1.0
	v_pk_fma_f16 v138, v138, v138, -2.0 op_sel:[0,1,1] op_sel_hi:[1,1,0]
	s_waitcnt lgkmcnt(4)
	v_mfma_scale_f32_32x32x64_f8f6f4 v[64:79], v[236:243], v[128:135], v[64:79], v227, v226 op_sel_hi:[0,0,0]
	v_cvt_pk_f16_f32 v144, v146, v144
	v_cvt_scalef32_pk_fp8_f16 v139, v138, 1.0 op_sel:[0,0,1]
	v_pk_fma_f16 v146, v144, v144, -2.0 op_sel:[1,0,1] op_sel_hi:[1,1,0]
	v_cvt_scalef32_pk_fp8_f16 v138, v148, 1.0
	v_cvt_scalef32_pk_fp8_f16 v145, v144, 1.0
	v_pk_fma_f16 v147, v180, v180, -2.0 op_sel:[0,1,1] op_sel_hi:[1,1,0]
	v_pk_fma_f16 v148, v146, v146, -2.0 op_sel:[0,1,1] op_sel_hi:[1,1,0]
	v_cvt_scalef32_pk_fp8_f16 v138, v149, 1.0 op_sel:[0,0,1]
	v_cvt_scalef32_pk_fp8_f16 v144, v147, 1.0
	v_pk_fma_f16 v147, v147, v147, -2.0 op_sel:[0,1,1] op_sel_hi:[1,1,0]
	v_pk_fma_f16 v149, v148, v148, -2.0 op_sel:[0,1,1] op_sel_hi:[1,1,0]
	v_cvt_scalef32_pk_fp8_f16 v145, v146, 1.0 op_sel:[0,0,1]
	v_mfma_scale_f32_32x32x64_f8f6f4 v[80:95], v[236:243], v[152:159], v[80:95], v227, v226 op_sel_hi:[0,0,0]
	v_pk_fma_f16 v146, v149, v149, -2.0 op_sel:[0,1,1] op_sel_hi:[1,1,0]
	v_cvt_scalef32_pk_fp8_f16 v144, v147, 1.0 op_sel:[0,0,1]
	v_cvt_scalef32_pk_fp8_f16 v147, v146, 1.0
	v_pk_fma_f16 v146, v146, v146, -2.0 op_sel:[0,1,1] op_sel_hi:[1,1,0]
	v_sin_f32_e32 v150, v150
	v_cvt_scalef32_pk_fp8_f16 v147, v146, 1.0 op_sel:[0,0,1]
	v_cvt_scalef32_pk_fp8_f16 v146, v148, 1.0
	v_add_f32_e32 v148, v151, v151
	v_mul_f32_e32 v151, 0.15915494, v187
	v_cvt_scalef32_pk_fp8_f16 v146, v149, 1.0 op_sel:[0,0,1]
	v_cvt_pk_f16_f32 v149, v150, v148
	v_cvt_scalef32_pk_fp8_f16 v148, v149, 1.0
	s_waitcnt lgkmcnt(0)
	v_mfma_scale_f32_32x32x64_f8f6f4 v[0:15], v[162:169], v[128:135], v[0:15], v227, v226 op_sel_hi:[0,0,0]
	v_pk_fma_f16 v149, v149, v149, -2.0 op_sel:[1,0,1] op_sel_hi:[1,1,0]
	v_cvt_scalef32_pk_fp8_f16 v143, v160, 1.0 op_sel:[0,0,1]
	v_pk_fma_f16 v150, v149, v149, -2.0 op_sel:[0,1,1] op_sel_hi:[1,1,0]
	v_cvt_scalef32_pk_fp8_f16 v148, v149, 1.0 op_sel:[0,0,1]
	v_cvt_scalef32_pk_fp8_f16 v149, v150, 1.0
	v_mfma_scale_f32_32x32x64_f8f6f4 v[32:47], v[170:177], v[128:135], v[32:47], v227, v226 op_sel_hi:[0,0,0]
	v_cos_f32_e32 v128, v151
	v_sin_f32_e32 v129, v151
	v_pk_fma_f16 v130, v150, v150, -2.0 op_sel:[0,1,1] op_sel_hi:[1,1,0]
	v_add_f32_e32 v128, v128, v128
	v_cvt_pk_f16_f32 v128, v129, v128
	v_pk_fma_f16 v203, v128, v128, -2.0 op_sel:[1,0,1] op_sel_hi:[1,1,0]
	v_cvt_scalef32_pk_fp8_f16 v151, v128, 1.0
	v_pk_fma_f16 v128, v130, v130, -2.0 op_sel:[0,1,1] op_sel_hi:[1,1,0]
	s_nop 0
	v_cvt_scalef32_pk_fp8_f16 v150, v128, 1.0
	v_pk_fma_f16 v128, v128, v128, -2.0 op_sel:[0,1,1] op_sel_hi:[1,1,0]
	v_cvt_scalef32_pk_fp8_f16 v149, v130, 1.0 op_sel:[0,0,1]
	v_cvt_scalef32_pk_fp8_f16 v151, v203, 1.0 op_sel:[0,0,1]
	v_cvt_scalef32_pk_fp8_f16 v150, v128, 1.0 op_sel:[0,0,1]
	v_mfma_scale_f32_32x32x64_f8f6f4 v[48:63], v[170:177], v[152:159], v[48:63], v227, v226 op_sel_hi:[0,0,0]
	v_mfma_scale_f32_32x32x64_f8f6f4 v[16:31], v[162:169], v[152:159], v[16:31], v227, v226 op_sel_hi:[0,0,0]
	v_pk_fma_f16 v130, v160, v160, -2.0 op_sel:[0,1,1] op_sel_hi:[1,1,0]
	s_nop 0
	v_pk_fma_f16 v131, v130, v130, -2.0 op_sel:[0,1,1] op_sel_hi:[1,1,0]
	ds_read_b128 v[152:155], v234 offset:24576
	ds_read_b128 v[156:159], v234 offset:25600
	ds_read_b128 v[162:165], v234 offset:26624
	ds_read_b128 v[166:169], v234 offset:27648
	v_pk_fma_f16 v128, v131, v131, -2.0 op_sel:[0,1,1] op_sel_hi:[1,1,0]
	v_mov_b32_e32 v160, v204
	v_pk_fma_f16 v132, v128, v128, -2.0 op_sel:[0,1,1] op_sel_hi:[1,1,0]
	v_cvt_scalef32_pk_fp8_f16 v129, v128, 1.0
	v_cvt_scalef32_pk_fp8_f16 v129, v132, 1.0 op_sel:[0,0,1]
	v_mul_f32_e32 v132, 0.15915494, v179
	v_sin_f32_e32 v133, v132
	v_cos_f32_e32 v132, v132
	v_cvt_scalef32_pk_fp8_f16 v128, v130, 1.0
	v_cvt_scalef32_pk_fp8_f16 v128, v131, 1.0 op_sel:[0,0,1]
	v_add_f32_e32 v130, v132, v132
	v_cvt_pk_f16_f32 v132, v133, v130
	v_pk_fma_f16 v133, v132, v132, -2.0 op_sel:[1,0,1] op_sel_hi:[1,1,0]
	s_nop 0
	v_pk_fma_f16 v130, v133, v133, -2.0 op_sel:[0,1,1] op_sel_hi:[1,1,0]
	s_waitcnt lgkmcnt(2)
	v_mfma_scale_f32_32x32x64_f8f6f4 v[96:111], v[152:159], v[136:143], v[96:111], v227, v226 op_sel_hi:[0,0,0]
	v_cvt_scalef32_pk_fp8_f16 v131, v130, 1.0
	v_pk_fma_f16 v134, v130, v130, -2.0 op_sel:[0,1,1] op_sel_hi:[1,1,0]
	v_cvt_scalef32_pk_fp8_f16 v130, v132, 1.0
	v_cvt_scalef32_pk_fp8_f16 v131, v134, 1.0 op_sel:[0,0,1]
	v_cvt_scalef32_pk_fp8_f16 v130, v133, 1.0 op_sel:[0,0,1]
	v_pk_fma_f16 v133, v134, v134, -2.0 op_sel:[0,1,1] op_sel_hi:[1,1,0]
	v_mul_f32_e32 v134, 0.15915494, v181
	v_cos_f32_e32 v135, v134
	v_sin_f32_e32 v134, v134
	v_cvt_scalef32_pk_fp8_f16 v132, v133, 1.0
	v_pk_fma_f16 v133, v133, v133, -2.0 op_sel:[0,1,1] op_sel_hi:[1,1,0]
	ds_read_b128 v[170:173], v234 offset:28672
	ds_read_b128 v[174:177], v234 offset:29696
	ds_read_b128 v[236:239], v234 offset:30720
	ds_read_b128 v[240:243], v234 offset:31744
	v_cvt_scalef32_pk_fp8_f16 v132, v133, 1.0 op_sel:[0,0,1]
	v_add_f32_e32 v133, v135, v135
	v_mfma_scale_f32_32x32x64_f8f6f4 v[112:127], v[152:159], v[144:151], v[112:127], v227, v226 op_sel_hi:[0,0,0]
	v_cvt_pk_f16_f32 v152, v134, v133
	v_mul_f32_e32 v153, 0.15915494, v188
	v_lshl_add_u64 v[134:135], v[160:161], 2, s[4:5]
	v_mul_f32_e32 v154, 0.15915494, v189
	global_load_dwordx4 v[178:181], v[134:135], off offset:32
	global_load_dwordx4 v[186:189], v[134:135], off offset:3488
	v_pk_fma_f16 v134, v152, v152, -2.0 op_sel:[1,0,1] op_sel_hi:[1,1,0]
	v_cvt_scalef32_pk_fp8_f16 v133, v152, 1.0
	v_pk_fma_f16 v152, v134, v134, -2.0 op_sel:[0,1,1] op_sel_hi:[1,1,0]
	v_cvt_scalef32_pk_fp8_f16 v133, v134, 1.0 op_sel:[0,0,1]
	v_pk_fma_f16 v155, v152, v152, -2.0 op_sel:[0,1,1] op_sel_hi:[1,1,0]
	s_nop 0
	v_pk_fma_f16 v134, v155, v155, -2.0 op_sel:[0,1,1] op_sel_hi:[1,1,0]
	s_nop 0
	v_pk_fma_f16 v156, v134, v134, -2.0 op_sel:[0,1,1] op_sel_hi:[1,1,0]
	v_cvt_scalef32_pk_fp8_f16 v135, v134, 1.0
	v_cvt_scalef32_pk_fp8_f16 v134, v152, 1.0
	v_pk_fma_f16 v152, v203, v203, -2.0 op_sel:[0,1,1] op_sel_hi:[1,1,0]
	v_cvt_scalef32_pk_fp8_f16 v134, v155, 1.0 op_sel:[0,0,1]
	v_pk_fma_f16 v155, v152, v152, -2.0 op_sel:[0,1,1] op_sel_hi:[1,1,0]
	s_waitcnt lgkmcnt(4)
	v_mfma_scale_f32_32x32x64_f8f6f4 v[64:79], v[162:169], v[136:143], v[64:79], v227, v226 op_sel_hi:[0,0,0]
	v_cvt_scalef32_pk_fp8_f16 v135, v156, 1.0 op_sel:[0,0,1]
	v_pk_fma_f16 v156, v155, v155, -2.0 op_sel:[0,1,1] op_sel_hi:[1,1,0]
	s_nop 0
	v_pk_fma_f16 v157, v156, v156, -2.0 op_sel:[0,1,1] op_sel_hi:[1,1,0]
	v_mfma_scale_f32_32x32x64_f8f6f4 v[80:95], v[162:169], v[144:151], v[80:95], v227, v226 op_sel_hi:[0,0,0]
	v_cvt_scalef32_pk_fp8_f16 v165, v156, 1.0
	v_cos_f32_e32 v156, v153
	v_sin_f32_e32 v153, v153
	v_cvt_scalef32_pk_fp8_f16 v164, v152, 1.0
	v_add_f32_e32 v152, v156, v156
	v_cvt_pk_f16_f32 v152, v153, v152
	v_pk_fma_f16 v153, v152, v152, -2.0 op_sel:[1,0,1] op_sel_hi:[1,1,0]
	v_cvt_scalef32_pk_fp8_f16 v166, v152, 1.0
	v_cvt_scalef32_pk_fp8_f16 v164, v155, 1.0 op_sel:[0,0,1]
	v_pk_fma_f16 v155, v153, v153, -2.0 op_sel:[0,1,1] op_sel_hi:[1,1,0]
	v_cvt_scalef32_pk_fp8_f16 v166, v153, 1.0 op_sel:[0,0,1]
	s_waitcnt lgkmcnt(0)
	v_mfma_scale_f32_32x32x64_f8f6f4 v[0:15], v[236:243], v[136:143], v[0:15], v227, v226 op_sel_hi:[0,0,0]
	v_cos_f32_e32 v153, v154
	v_cvt_scalef32_pk_fp8_f16 v167, v155, 1.0
	v_pk_fma_f16 v155, v155, v155, -2.0 op_sel:[0,1,1] op_sel_hi:[1,1,0]
	v_sin_f32_e32 v154, v154
	v_pk_fma_f16 v152, v155, v155, -2.0 op_sel:[0,1,1] op_sel_hi:[1,1,0]
	s_nop 0
	v_cvt_scalef32_pk_fp8_f16 v168, v152, 1.0
	v_pk_fma_f16 v152, v152, v152, -2.0 op_sel:[0,1,1] op_sel_hi:[1,1,0]
	s_nop 0
	v_cvt_scalef32_pk_fp8_f16 v168, v152, 1.0 op_sel:[0,0,1]
	v_add_f32_e32 v152, v153, v153
	v_cvt_scalef32_pk_fp8_f16 v165, v157, 1.0 op_sel:[0,0,1]
	v_cvt_scalef32_pk_fp8_f16 v167, v155, 1.0 op_sel:[0,0,1]
	v_mfma_scale_f32_32x32x64_f8f6f4 v[32:47], v[170:177], v[136:143], v[32:47], v227, v226 op_sel_hi:[0,0,0]
	v_cvt_pk_f16_f32 v136, v154, v152
	v_cvt_scalef32_pk_fp8_f16 v169, v136, 1.0
	v_pk_fma_f16 v136, v136, v136, -2.0 op_sel:[1,0,1] op_sel_hi:[1,1,0]
	s_nop 0
	v_cvt_scalef32_pk_fp8_f16 v169, v136, 1.0 op_sel:[0,0,1]
	v_pk_fma_f16 v136, v136, v136, -2.0 op_sel:[0,1,1] op_sel_hi:[1,1,0]
	s_nop 0
	v_pk_fma_f16 v137, v136, v136, -2.0 op_sel:[0,1,1] op_sel_hi:[1,1,0]
	s_nop 0
	v_pk_fma_f16 v138, v137, v137, -2.0 op_sel:[0,1,1] op_sel_hi:[1,1,0]
	s_nop 0
	v_pk_fma_f16 v139, v138, v138, -2.0 op_sel:[0,1,1] op_sel_hi:[1,1,0]
	v_mfma_scale_f32_32x32x64_f8f6f4 v[48:63], v[170:177], v[144:151], v[48:63], v227, v226 op_sel_hi:[0,0,0]
	v_cvt_scalef32_pk_fp8_f16 v171, v138, 1.0
	v_cvt_scalef32_pk_fp8_f16 v170, v136, 1.0
	v_cvt_scalef32_pk_fp8_f16 v171, v139, 1.0 op_sel:[0,0,1]
	v_cvt_scalef32_pk_fp8_f16 v170, v137, 1.0 op_sel:[0,0,1]
	v_mfma_scale_f32_32x32x64_f8f6f4 v[16:31], v[236:243], v[144:151], v[16:31], v227, v226 op_sel_hi:[0,0,0]
	v_mul_f32_e32 v152, 0.15915494, v225
	ds_read_b128 v[136:139], v234 offset:32768
	ds_read_b128 v[140:143], v234 offset:33792
	v_cos_f32_e32 v153, v152
	v_sin_f32_e32 v152, v152
	v_mov_b32_e32 v205, v161
	s_waitcnt lgkmcnt(0)
	v_mfma_scale_f32_32x32x64_f8f6f4 v[96:111], v[136:143], v[128:135], v[96:111], v227, v226 op_sel_hi:[0,0,0]
	v_add_f32_e32 v153, v153, v153
	v_cvt_pk_f16_f32 v158, v152, v153
	v_mov_b32_e32 v203, v161
	v_cndmask_b32_e64 v162, 0, v222, s[0:1]
	v_mul_f32_e32 v163, 0.15915494, v223
	v_pk_fma_f16 v159, v158, v158, -2.0 op_sel:[1,0,1] op_sel_hi:[1,1,0]
	v_cndmask_b32_e64 v172, 0, v224, s[0:1]
	v_pk_fma_f16 v156, v159, v159, -2.0 op_sel:[0,1,1] op_sel_hi:[1,1,0]
	s_nop 0
	v_pk_fma_f16 v160, v156, v156, -2.0 op_sel:[0,1,1] op_sel_hi:[1,1,0]
	v_cvt_scalef32_pk_fp8_f16 v157, v156, 1.0
	v_cvt_scalef32_pk_fp8_f16 v156, v158, 1.0
	v_cvt_scalef32_pk_fp8_f16 v156, v159, 1.0 op_sel:[0,0,1]
	v_mfma_scale_f32_32x32x64_f8f6f4 v[112:127], v[136:143], v[164:171], v[112:127], v227, v226 op_sel_hi:[0,0,0]
	ds_read_b128 v[136:139], v234 offset:34816
	ds_read_b128 v[140:143], v234 offset:35840
	ds_read_b128 v[144:147], v234 offset:36864
	ds_read_b128 v[148:151], v234 offset:37888
	ds_read_b128 v[236:239], v234 offset:38912
	ds_read_b128 v[240:243], v234 offset:39936
	v_lshl_add_u64 v[152:153], v[204:205], 2, s[4:5]
	v_lshl_add_u64 v[154:155], v[202:203], 2, s[4:5]
	global_load_dword v225, v[152:153], off offset:48
	global_load_dword v222, v[154:155], off
	global_load_dword v224, v[154:155], off offset:3456
	global_load_dword v223, v[152:153], off offset:3504
	v_cvt_scalef32_pk_fp8_f16 v157, v160, 1.0 op_sel:[0,0,1]
	s_waitcnt lgkmcnt(4)
	v_mfma_scale_f32_32x32x64_f8f6f4 v[64:79], v[136:143], v[128:135], v[64:79], v227, v226 op_sel_hi:[0,0,0]
	v_mfma_scale_f32_32x32x64_f8f6f4 v[80:95], v[136:143], v[164:171], v[80:95], v227, v226 op_sel_hi:[0,0,0]
	v_mul_f32_e32 v136, v207, v208
	v_fma_f32 v137, v208, v208, -2.0
	v_cndmask_b32_e64 v138, v137, v136, s[0:1]
	v_mul_f32_e32 v136, v136, v137
	v_fma_f32 v137, v137, v137, -2.0
	v_cndmask_b32_e64 v139, v137, v136, s[0:1]
	v_cvt_pk_fp8_f32 v159, v138, v139
	v_mul_f32_e32 v136, v136, v137
	v_fma_f32 v137, v137, v137, -2.0
	v_cndmask_b32_e64 v136, v137, v136, s[0:1]
	v_cvt_pk_fp8_f32 v159, v136, v162 op_sel:[0,0,1]
	v_pk_fma_f16 v136, v160, v160, -2.0 op_sel:[0,1,1] op_sel_hi:[1,1,0]
	v_mov_b32_e32 v160, v161
	v_pk_fma_f16 v137, v136, v136, -2.0 op_sel:[0,1,1] op_sel_hi:[1,1,0]
	v_cvt_scalef32_pk_fp8_f16 v158, v136, 1.0
	v_cos_f32_e32 v136, v163
	v_cvt_scalef32_pk_fp8_f16 v158, v137, 1.0 op_sel:[0,0,1]
	v_sin_f32_e32 v137, v163
	s_waitcnt lgkmcnt(0)
	v_mfma_scale_f32_32x32x64_f8f6f4 v[0:15], v[236:243], v[128:135], v[0:15], v227, v226 op_sel_hi:[0,0,0]
	v_add_f32_e32 v136, v136, v136
	v_mov_b32_e32 v162, v161
	v_cvt_pk_f16_f32 v138, v137, v136
	v_pk_fma_f16 v139, v138, v138, -2.0 op_sel:[1,0,1] op_sel_hi:[1,1,0]
	s_nop 0
	v_pk_fma_f16 v136, v139, v139, -2.0 op_sel:[0,1,1] op_sel_hi:[1,1,0]
	v_mov_b32_e32 v163, v161
	v_pk_fma_f16 v140, v136, v136, -2.0 op_sel:[0,1,1] op_sel_hi:[1,1,0]
	v_cvt_scalef32_pk_fp8_f16 v137, v136, 1.0
	v_cvt_scalef32_pk_fp8_f16 v136, v138, 1.0
	v_cvt_scalef32_pk_fp8_f16 v136, v139, 1.0 op_sel:[0,0,1]
	v_mul_f32_e32 v138, v209, v210
	v_fma_f32 v139, v210, v210, -2.0
	v_cndmask_b32_e64 v141, v139, v138, s[0:1]
	v_mul_f32_e32 v138, v138, v139
	v_fma_f32 v142, v139, v139, -2.0
	v_cndmask_b32_e64 v143, v142, v138, s[0:1]
	v_cvt_pk_fp8_f32 v139, v141, v143
	v_mfma_scale_f32_32x32x64_f8f6f4 v[32:47], v[144:151], v[128:135], v[32:47], v227, v226 op_sel_hi:[0,0,0]
	v_mul_f32_e32 v128, v138, v142
	v_fma_f32 v129, v142, v142, -2.0
	v_cndmask_b32_e64 v128, v129, v128, s[0:1]
	v_cvt_pk_fp8_f32 v139, v128, v172 op_sel:[0,0,1]
	v_pk_fma_f16 v128, v140, v140, -2.0 op_sel:[0,1,1] op_sel_hi:[1,1,0]
	s_nop 0
	v_cvt_scalef32_pk_fp8_f16 v138, v128, 1.0
	v_pk_fma_f16 v128, v128, v128, -2.0 op_sel:[0,1,1] op_sel_hi:[1,1,0]
	v_cvt_scalef32_pk_fp8_f16 v137, v140, 1.0 op_sel:[0,0,1]
	v_cvt_scalef32_pk_fp8_f16 v138, v128, 1.0 op_sel:[0,0,1]
	v_mov_b32_e32 v140, v161
	v_mov_b32_e32 v141, v161
	v_mov_b32_e32 v142, v161
	v_mov_b32_e32 v143, v161
	v_mfma_scale_f32_32x32x64_f8f6f4 v[48:63], v[144:151], v[164:171], v[48:63], v227, v226 op_sel_hi:[0,0,0]
	v_mfma_scale_f32_32x32x64_f8f6f4 v[16:31], v[236:243], v[164:171], v[16:31], v227, v226 op_sel_hi:[0,0,0]
	ds_read_b128 v[128:131], v234 offset:40960
	ds_read_b128 v[132:135], v234 offset:41984
	s_waitcnt lgkmcnt(0)
	v_mfma_scale_f32_32x32x64_f8f6f4 v[96:111], v[128:135], v[156:163], v[96:111], v227, v226 op_sel_hi:[0,0,0]
	v_mfma_scale_f32_32x32x64_f8f6f4 v[112:127], v[128:135], v[136:143], v[112:127], v227, v226 op_sel_hi:[0,0,0]
	ds_read_b128 v[128:131], v234 offset:43008
	ds_read_b128 v[132:135], v234 offset:44032
	s_waitcnt lgkmcnt(0)
	v_mfma_scale_f32_32x32x64_f8f6f4 v[64:79], v[128:135], v[156:163], v[64:79], v227, v226 op_sel_hi:[0,0,0]
	v_mfma_scale_f32_32x32x64_f8f6f4 v[80:95], v[128:135], v[136:143], v[80:95], v227, v226 op_sel_hi:[0,0,0]
	ds_read_b128 v[128:131], v234 offset:45056
	ds_read_b128 v[132:135], v234 offset:46080
	s_waitcnt lgkmcnt(0)
	v_mfma_scale_f32_32x32x64_f8f6f4 v[32:47], v[128:135], v[156:163], v[32:47], v227, v226 op_sel_hi:[0,0,0]
	v_mfma_scale_f32_32x32x64_f8f6f4 v[48:63], v[128:135], v[136:143], v[48:63], v227, v226 op_sel_hi:[0,0,0]
	ds_read_b128 v[128:131], v234 offset:47104
	ds_read_b128 v[132:135], v234 offset:48128
	ds_read_b128 v[174:177], v234 offset:49152
	ds_read_b128 v[208:211], v234 offset:50176
	ds_read_b128 v[212:215], v234 offset:53248
	ds_read_b128 v[236:239], v234 offset:54272
	s_waitcnt lgkmcnt(4)
	v_mfma_scale_f32_32x32x64_f8f6f4 v[0:15], v[128:135], v[156:163], v[0:15], v227, v226 op_sel_hi:[0,0,0]
	v_mfma_scale_f32_32x32x64_f8f6f4 v[16:31], v[128:135], v[136:143], v[16:31], v227, v226 op_sel_hi:[0,0,0]
	v_cvt_pk_bf16_f32 v96, v96, v97
	v_pk_max_i16 v162, v96, 0
	v_cvt_pk_bf16_f32 v96, v98, v99
	v_pk_max_i16 v163, v96, 0
	v_cvt_pk_bf16_f32 v96, v100, v101
	v_pk_max_i16 v164, v96, 0
	v_cvt_pk_bf16_f32 v96, v102, v103
	v_pk_max_i16 v165, v96, 0
	v_cvt_pk_bf16_f32 v96, v112, v113
	v_pk_max_i16 v166, v96, 0
	v_cvt_pk_bf16_f32 v96, v114, v115
	v_pk_max_i16 v167, v96, 0
	v_cvt_pk_bf16_f32 v96, v116, v117
	v_pk_max_i16 v168, v96, 0
	v_cvt_pk_bf16_f32 v96, v118, v119
	v_pk_max_i16 v169, v96, 0
	v_cvt_pk_bf16_f32 v96, v104, v105
	v_pk_max_i16 v170, v96, 0
	v_cvt_pk_bf16_f32 v96, v106, v107
	v_pk_max_i16 v171, v96, 0
	v_cvt_pk_bf16_f32 v96, v108, v109
	v_add_u32_e32 v128, 0, v206
	v_pk_max_i16 v172, v96, 0
	v_cvt_pk_bf16_f32 v96, v110, v111
	v_add_u32_e32 v235, 0x18000, v128
	v_pk_max_i16 v173, v96, 0
	v_cvt_pk_bf16_f32 v96, v120, v121
	ds_read_b128 v[128:131], v235
	ds_read_b128 v[132:135], v235 offset:32
	ds_read_b128 v[136:139], v235 offset:64
	ds_read_b128 v[140:143], v235 offset:96
	v_pk_max_i16 v202, v96, 0
	v_cvt_pk_bf16_f32 v96, v122, v123
	v_pk_max_i16 v203, v96, 0
	ds_read_b128 v[96:99], v235 offset:128
	ds_read_b128 v[100:103], v235 offset:160
	ds_read_b128 v[104:107], v235 offset:192
	ds_read_b128 v[108:111], v235 offset:224
	v_cvt_pk_bf16_f32 v112, v124, v125
	v_cvt_pk_bf16_f32 v64, v64, v65
	s_waitcnt lgkmcnt(4)
	v_mfma_f32_32x32x16_bf16 v[144:159], v[174:177], v[166:169], v[128:143]
	v_pk_max_i16 v204, v112, 0
	v_cvt_pk_bf16_f32 v112, v126, v127
	v_pk_max_i16 v205, v112, 0
	ds_read_b128 v[240:243], v234 offset:57344
	ds_read_b128 v[244:247], v234 offset:58368
	ds_read_b128 v[248:251], v234 offset:61440
	ds_read_b128 v[252:255], v234 offset:62464
	v_cvt_pk_bf16_f32 v65, v74, v75
	v_cndmask_b32_e64 v230, v230, 0, s[14:15]
	v_pk_max_i16 v65, v65, 0
	v_mfma_f32_32x32x16_bf16 v[128:143], v[174:177], v[162:165], v[128:143]
	v_pk_max_i16 v174, v64, 0
	v_cvt_pk_bf16_f32 v64, v66, v67
	v_pk_max_i16 v175, v64, 0
	v_cvt_pk_bf16_f32 v64, v68, v69
	v_pk_max_i16 v176, v64, 0
	v_cvt_pk_bf16_f32 v64, v70, v71
	v_pk_max_i16 v177, v64, 0
	s_waitcnt lgkmcnt(4)
	v_mfma_f32_32x32x16_bf16 v[112:127], v[208:211], v[166:169], v[96:111]
	v_cvt_pk_bf16_f32 v64, v80, v81
	v_pk_max_i16 v80, v64, 0
	v_cvt_pk_bf16_f32 v64, v82, v83
	v_pk_max_i16 v81, v64, 0
	v_cvt_pk_bf16_f32 v64, v84, v85
	v_pk_max_i16 v82, v64, 0
	v_cvt_pk_bf16_f32 v64, v86, v87
	v_mfma_f32_32x32x16_bf16 v[96:111], v[208:211], v[162:165], v[96:111]
	v_pk_max_i16 v83, v64, 0
	v_cvt_pk_bf16_f32 v64, v72, v73
	v_cvt_pk_bf16_f32 v66, v76, v77
	v_pk_max_i16 v64, v64, 0
	v_pk_max_i16 v66, v66, 0
	v_cvt_pk_bf16_f32 v67, v78, v79
	v_cvt_pk_bf16_f32 v68, v88, v89
	v_cvt_pk_bf16_f32 v69, v90, v91
	v_cvt_pk_bf16_f32 v70, v92, v93
	v_cvt_pk_bf16_f32 v71, v94, v95
	v_add_u32_e32 v160, 0x14000, v234
	v_mfma_f32_32x32x16_bf16 v[128:143], v[212:215], v[170:173], v[128:143]
	v_pk_max_i16 v67, v67, 0
	v_pk_max_i16 v68, v68, 0
	v_pk_max_i16 v69, v69, 0
	v_pk_max_i16 v70, v70, 0
	v_pk_max_i16 v71, v71, 0
	v_mfma_f32_32x32x16_bf16 v[144:159], v[212:215], v[202:205], v[144:159]
	v_mfma_f32_32x32x16_bf16 v[96:111], v[236:239], v[170:173], v[96:111]
	v_mfma_f32_32x32x16_bf16 v[112:127], v[236:239], v[202:205], v[112:127]
	v_cvt_pk_bf16_f32 v32, v32, v33
	v_pk_max_i16 v76, v32, 0
	v_cvt_pk_bf16_f32 v32, v34, v35
	v_pk_max_i16 v77, v32, 0
	v_cvt_pk_bf16_f32 v32, v36, v37
	v_pk_max_i16 v78, v32, 0
	v_cvt_pk_bf16_f32 v32, v38, v39
	v_pk_max_i16 v79, v32, 0
	v_cvt_pk_bf16_f32 v32, v48, v49
	v_pk_max_i16 v88, v32, 0
	v_cvt_pk_bf16_f32 v32, v50, v51
	v_pk_max_i16 v89, v32, 0
	v_cvt_pk_bf16_f32 v32, v52, v53
	v_pk_max_i16 v90, v32, 0
	v_cvt_pk_bf16_f32 v32, v54, v55
	s_waitcnt lgkmcnt(3)
	v_mfma_f32_32x32x16_bf16 v[128:143], v[240:243], v[174:177], v[128:143]
	v_pk_max_i16 v91, v32, 0
	v_cvt_pk_bf16_f32 v32, v40, v41
	v_pk_max_i16 v72, v32, 0
	v_cvt_pk_bf16_f32 v32, v42, v43
	v_pk_max_i16 v73, v32, 0
	v_cvt_pk_bf16_f32 v32, v44, v45
	v_pk_max_i16 v74, v32, 0
	v_mfma_f32_32x32x16_bf16 v[144:159], v[240:243], v[80:83], v[144:159]
	ds_read_b128 v[92:95], v233 offset:16384
	ds_read_b128 v[208:211], v233 offset:17408
	ds_read_b128 v[236:239], v233 offset:20480
	ds_read_b128 v[240:243], v233 offset:21504
	v_cvt_pk_bf16_f32 v32, v46, v47
	v_pk_max_i16 v75, v32, 0
	v_cvt_pk_bf16_f32 v32, v56, v57
	v_pk_max_i16 v84, v32, 0
	v_cvt_pk_bf16_f32 v32, v58, v59
	v_pk_max_i16 v85, v32, 0
	s_waitcnt lgkmcnt(6)
	v_mfma_f32_32x32x16_bf16 v[96:111], v[244:247], v[174:177], v[96:111]
	v_cvt_pk_bf16_f32 v32, v60, v61
	v_pk_max_i16 v86, v32, 0
	v_cvt_pk_bf16_f32 v32, v62, v63
	v_pk_max_i16 v87, v32, 0
	v_mfma_f32_32x32x16_bf16 v[112:127], v[244:247], v[80:83], v[112:127]
	s_waitcnt lgkmcnt(5)
	v_mfma_f32_32x32x16_bf16 v[128:143], v[248:251], v[64:67], v[128:143]
	v_mfma_f32_32x32x16_bf16 v[144:159], v[248:251], v[68:71], v[144:159]
	s_waitcnt lgkmcnt(4)
	v_mfma_f32_32x32x16_bf16 v[96:111], v[252:255], v[64:67], v[96:111]
	v_mfma_f32_32x32x16_bf16 v[112:127], v[252:255], v[68:71], v[112:127]
	v_cvt_pk_bf16_f32 v0, v0, v1
	v_pk_max_i16 v206, v0, 0
	v_cvt_pk_bf16_f32 v0, v2, v3
	v_pk_max_i16 v207, v0, 0
	v_cvt_pk_bf16_f32 v0, v4, v5
	s_waitcnt lgkmcnt(2)
	v_mfma_f32_32x32x16_bf16 v[96:111], v[208:211], v[76:79], v[96:111]
	ds_read_b128 v[32:35], v233 offset:24576
	ds_read_b128 v[36:39], v233 offset:25600
	ds_read_b128 v[40:43], v233 offset:28672
	ds_read_b128 v[44:47], v233 offset:29696
	v_mfma_f32_32x32x16_bf16 v[112:127], v[208:211], v[88:91], v[112:127]
	v_pk_max_i16 v208, v0, 0
	v_cvt_pk_bf16_f32 v0, v6, v7
	v_pk_max_i16 v209, v0, 0
	v_cvt_pk_bf16_f32 v0, v16, v17
	v_pk_max_i16 v214, v0, 0
	v_cvt_pk_bf16_f32 v0, v18, v19
	v_pk_max_i16 v215, v0, 0
	v_cvt_pk_bf16_f32 v0, v20, v21
	v_pk_max_i16 v216, v0, 0
	v_cvt_pk_bf16_f32 v0, v22, v23
	v_mfma_f32_32x32x16_bf16 v[128:143], v[92:95], v[76:79], v[128:143]
	v_pk_max_i16 v217, v0, 0
	v_cvt_pk_bf16_f32 v0, v8, v9
	v_mfma_f32_32x32x16_bf16 v[144:159], v[92:95], v[88:91], v[144:159]
	v_pk_max_i16 v92, v0, 0
	v_cvt_pk_bf16_f32 v0, v10, v11
	v_pk_max_i16 v93, v0, 0
	v_cvt_pk_bf16_f32 v0, v12, v13
	v_pk_max_i16 v94, v0, 0
	v_cvt_pk_bf16_f32 v0, v14, v15
	v_pk_max_i16 v95, v0, 0
	v_cvt_pk_bf16_f32 v0, v24, v25
	v_pk_max_i16 v210, v0, 0
	v_cvt_pk_bf16_f32 v0, v26, v27
	v_pk_max_i16 v211, v0, 0
	v_cvt_pk_bf16_f32 v0, v28, v29
	v_pk_max_i16 v212, v0, 0
	v_cvt_pk_bf16_f32 v0, v30, v31
	s_waitcnt lgkmcnt(5)
	v_mfma_f32_32x32x16_bf16 v[128:143], v[236:239], v[72:75], v[128:143]
	v_pk_max_i16 v213, v0, 0
	v_mfma_f32_32x32x16_bf16 v[144:159], v[236:239], v[84:87], v[144:159]
	s_waitcnt lgkmcnt(4)
	v_mfma_f32_32x32x16_bf16 v[96:111], v[240:243], v[72:75], v[96:111]
	v_mfma_f32_32x32x16_bf16 v[112:127], v[240:243], v[84:87], v[112:127]
	s_waitcnt lgkmcnt(3)
	v_mfma_f32_32x32x16_bf16 v[128:143], v[32:35], v[206:209], v[128:143]
	ds_read_b128 v[0:3], v234 offset:51200
	ds_read_b128 v[236:239], v234 offset:52224
	ds_read_b128 v[240:243], v234 offset:55296
	ds_read_b128 v[244:247], v234 offset:56320
	v_mfma_f32_32x32x16_bf16 v[144:159], v[32:35], v[214:217], v[144:159]
	s_waitcnt lgkmcnt(6)
	v_mfma_f32_32x32x16_bf16 v[96:111], v[36:39], v[206:209], v[96:111]
	v_mfma_f32_32x32x16_bf16 v[112:127], v[36:39], v[214:217], v[112:127]
	s_waitcnt lgkmcnt(5)
	v_mfma_f32_32x32x16_bf16 v[128:143], v[40:43], v[92:95], v[128:143]
	v_mfma_f32_32x32x16_bf16 v[144:159], v[40:43], v[210:213], v[144:159]
	s_waitcnt lgkmcnt(4)
	v_mfma_f32_32x32x16_bf16 v[96:111], v[44:47], v[92:95], v[96:111]
	v_mfma_f32_32x32x16_bf16 v[112:127], v[44:47], v[210:213], v[112:127]
	ds_read_b128 v[32:35], v235 offset:256
	ds_read_b128 v[36:39], v235 offset:288
	ds_read_b128 v[40:43], v235 offset:320
	ds_read_b128 v[44:47], v235 offset:352
	s_nop 3
	v_cvt_pk_bf16_f32 v128, v128, v129
	v_cvt_pk_bf16_f32 v129, v130, v131
	v_cvt_pk_bf16_f32 v130, v132, v133
	v_cvt_pk_bf16_f32 v131, v134, v135
	s_waitcnt lgkmcnt(0)
	v_mfma_f32_32x32x16_bf16 v[48:63], v[0:3], v[166:169], v[32:47]
	v_cvt_pk_bf16_f32 v132, v144, v145
	v_cvt_pk_bf16_f32 v133, v146, v147
	v_cvt_pk_bf16_f32 v134, v148, v149
	v_cvt_pk_bf16_f32 v135, v150, v151
	v_pk_max_i16 v128, v128, 0
	v_pk_max_i16 v129, v129, 0
	v_pk_max_i16 v130, v130, 0
	v_mfma_f32_32x32x16_bf16 v[32:47], v[0:3], v[162:165], v[32:47]
	ds_read_b128 v[0:3], v235 offset:384
	ds_read_b128 v[4:7], v235 offset:416
	ds_read_b128 v[8:11], v235 offset:448
	ds_read_b128 v[12:15], v235 offset:480
	v_pk_max_i16 v131, v131, 0
	v_pk_max_i16 v132, v132, 0
	v_pk_max_i16 v133, v133, 0
	v_pk_max_i16 v134, v134, 0
	v_pk_max_i16 v135, v135, 0
	s_waitcnt lgkmcnt(0)
	v_mfma_f32_32x32x16_bf16 v[16:31], v[236:239], v[166:169], v[0:15]
	v_mfma_f32_32x32x16_bf16 v[0:15], v[236:239], v[162:165], v[0:15]
	ds_read_b128 v[162:165], v234 offset:59392
	ds_read_b128 v[166:169], v234 offset:60416
	ds_read_b128 v[236:239], v234 offset:63488
	ds_read_b128 v[248:251], v234 offset:64512
	v_mfma_f32_32x32x16_bf16 v[0:15], v[244:247], v[170:173], v[0:15]
	v_mfma_f32_32x32x16_bf16 v[32:47], v[240:243], v[170:173], v[32:47]
	v_mfma_f32_32x32x16_bf16 v[48:63], v[240:243], v[202:205], v[48:63]
	v_mfma_f32_32x32x16_bf16 v[16:31], v[244:247], v[202:205], v[16:31]
	s_waitcnt lgkmcnt(2)
	v_mfma_f32_32x32x16_bf16 v[0:15], v[166:169], v[174:177], v[0:15]
	v_cvt_pk_bf16_f32 v136, v136, v137
	v_cvt_pk_bf16_f32 v137, v138, v139
	v_cvt_pk_bf16_f32 v138, v140, v141
	v_cvt_pk_bf16_f32 v139, v142, v143
	v_cvt_pk_bf16_f32 v140, v152, v153
	v_pk_max_i16 v136, v136, 0
	v_pk_max_i16 v137, v137, 0
	v_mfma_f32_32x32x16_bf16 v[32:47], v[162:165], v[174:177], v[32:47]
	v_pk_max_i16 v138, v138, 0
	v_pk_max_i16 v139, v139, 0
	v_pk_max_i16 v140, v140, 0
	v_mfma_f32_32x32x16_bf16 v[48:63], v[162:165], v[80:83], v[48:63]
	v_mfma_f32_32x32x16_bf16 v[16:31], v[166:169], v[80:83], v[16:31]
	ds_read_b128 v[80:83], v233 offset:18432
	ds_read_b128 v[144:147], v233 offset:19456
	ds_read_b128 v[148:151], v233 offset:22528
	ds_read_b128 v[162:165], v233 offset:23552
	s_waitcnt lgkmcnt(4)
	v_mfma_f32_32x32x16_bf16 v[0:15], v[248:251], v[64:67], v[0:15]
	v_mfma_f32_32x32x16_bf16 v[32:47], v[236:239], v[64:67], v[32:47]
	v_cvt_pk_bf16_f32 v64, v154, v155
	v_pk_max_i16 v141, v64, 0
	v_cvt_pk_bf16_f32 v64, v156, v157
	v_pk_max_i16 v142, v64, 0
	v_cvt_pk_bf16_f32 v64, v158, v159
	v_pk_max_i16 v143, v64, 0
	v_mfma_f32_32x32x16_bf16 v[48:63], v[236:239], v[68:71], v[48:63]
	v_mfma_f32_32x32x16_bf16 v[16:31], v[248:251], v[68:71], v[16:31]
	s_waitcnt lgkmcnt(2)
	v_mfma_f32_32x32x16_bf16 v[0:15], v[144:147], v[76:79], v[0:15]
	v_mfma_f32_32x32x16_bf16 v[32:47], v[80:83], v[76:79], v[32:47]
	v_mfma_f32_32x32x16_bf16 v[48:63], v[80:83], v[88:91], v[48:63]
	ds_read_b128 v[64:67], v233 offset:26624
	ds_read_b128 v[68:71], v233 offset:27648
	ds_read_b128 v[76:79], v233 offset:30720
	ds_read_b128 v[80:83], v233 offset:31744
	v_mfma_f32_32x32x16_bf16 v[16:31], v[144:147], v[88:91], v[16:31]
	v_cvt_pk_bf16_f32 v88, v96, v97
	v_pk_max_i16 v96, v88, 0
	v_cvt_pk_bf16_f32 v88, v98, v99
	v_pk_max_i16 v97, v88, 0
	v_cvt_pk_bf16_f32 v88, v100, v101
	v_pk_max_i16 v98, v88, 0
	v_cvt_pk_bf16_f32 v88, v102, v103
	s_waitcnt lgkmcnt(4)
	v_mfma_f32_32x32x16_bf16 v[0:15], v[162:165], v[72:75], v[0:15]
	v_pk_max_i16 v99, v88, 0
	v_cvt_pk_bf16_f32 v88, v112, v113
	v_pk_max_i16 v100, v88, 0
	v_mfma_f32_32x32x16_bf16 v[32:47], v[148:151], v[72:75], v[32:47]
	v_cvt_pk_bf16_f32 v72, v114, v115
	v_pk_max_i16 v101, v72, 0
	v_cvt_pk_bf16_f32 v72, v116, v117
	v_pk_max_i16 v102, v72, 0
	v_cvt_pk_bf16_f32 v72, v118, v119
	v_pk_max_i16 v103, v72, 0
	v_mfma_f32_32x32x16_bf16 v[48:63], v[148:151], v[84:87], v[48:63]
	v_mfma_f32_32x32x16_bf16 v[16:31], v[162:165], v[84:87], v[16:31]
	s_waitcnt lgkmcnt(2)
	v_mfma_f32_32x32x16_bf16 v[0:15], v[68:71], v[206:209], v[0:15]
	ds_read_b128 v[84:87], v160
	ds_read_b128 v[112:115], v160 offset:1024
	ds_read_b128 v[116:119], v160 offset:2048
	ds_read_b128 v[144:147], v160 offset:3072
	v_mfma_f32_32x32x16_bf16 v[32:47], v[64:67], v[206:209], v[32:47]
	v_mfma_f32_32x32x16_bf16 v[48:63], v[64:67], v[214:217], v[48:63]
	v_cvt_pk_bf16_f32 v64, v104, v105
	v_pk_max_i16 v104, v64, 0
	v_cvt_pk_bf16_f32 v64, v106, v107
	v_pk_max_i16 v105, v64, 0
	v_cvt_pk_bf16_f32 v64, v108, v109
	v_pk_max_i16 v106, v64, 0
	v_cvt_pk_bf16_f32 v64, v110, v111
	v_mfma_f32_32x32x16_bf16 v[16:31], v[68:71], v[214:217], v[16:31]
	v_pk_max_i16 v107, v64, 0
	v_cvt_pk_bf16_f32 v64, v120, v121
	v_pk_max_i16 v108, v64, 0
	v_cvt_pk_bf16_f32 v64, v122, v123
	v_pk_max_i16 v109, v64, 0
	v_cvt_pk_bf16_f32 v64, v124, v125
	v_pk_max_i16 v110, v64, 0
	s_waitcnt lgkmcnt(4)
	v_mfma_f32_32x32x16_bf16 v[0:15], v[80:83], v[92:95], v[0:15]
	v_cvt_pk_bf16_f32 v64, v126, v127
	v_pk_max_i16 v111, v64, 0
	v_mfma_f32_32x32x16_bf16 v[32:47], v[76:79], v[92:95], v[32:47]
	v_mfma_f32_32x32x16_bf16 v[48:63], v[76:79], v[210:213], v[48:63]
	v_mfma_f32_32x32x16_bf16 v[16:31], v[80:83], v[210:213], v[16:31]
	s_waitcnt lgkmcnt(3)
	v_mfma_f32_32x32x16_bf16 v[64:79], v[84:87], v[128:131], 0
	s_nop 7
	v_cvt_pk_bf16_f32 v32, v32, v33
	v_cvt_pk_bf16_f32 v33, v34, v35
	v_cvt_pk_bf16_f32 v34, v36, v37
	v_cvt_pk_bf16_f32 v35, v38, v39
	v_pk_max_i16 v32, v32, 0
	v_pk_max_i16 v33, v33, 0
	v_pk_max_i16 v34, v34, 0
	v_mfma_f32_32x32x16_bf16 v[80:95], v[84:87], v[132:135], 0
	v_pk_max_i16 v35, v35, 0
	v_cvt_pk_bf16_f32 v48, v48, v49
	v_cvt_pk_bf16_f32 v49, v50, v51
	v_cvt_pk_bf16_f32 v50, v52, v53
	v_cvt_pk_bf16_f32 v51, v54, v55
	v_pk_max_i16 v48, v48, 0
	v_pk_max_i16 v49, v49, 0
	s_waitcnt lgkmcnt(2)
	v_mfma_f32_32x32x16_bf16 v[64:79], v[112:115], v[136:139], v[64:79]
	v_pk_max_i16 v50, v50, 0
	v_pk_max_i16 v51, v51, 0
	v_cvt_pk_bf16_f32 v40, v40, v41
	v_cvt_pk_bf16_f32 v41, v42, v43
	v_cvt_pk_bf16_f32 v42, v44, v45
	v_cvt_pk_bf16_f32 v43, v46, v47
	v_pk_max_i16 v40, v40, 0
	v_mfma_f32_32x32x16_bf16 v[80:95], v[112:115], v[140:143], v[80:95]
	v_pk_max_i16 v41, v41, 0
	v_pk_max_i16 v42, v42, 0
	v_pk_max_i16 v43, v43, 0
	v_cvt_pk_bf16_f32 v52, v56, v57
	v_cvt_pk_bf16_f32 v53, v58, v59
	v_cvt_pk_bf16_f32 v54, v60, v61
	v_cvt_pk_bf16_f32 v55, v62, v63
	s_waitcnt lgkmcnt(1)
	v_mfma_f32_32x32x16_bf16 v[64:79], v[116:119], v[96:99], v[64:79]
	ds_read_b128 v[36:39], v160 offset:4096
	ds_read_b128 v[96:99], v160 offset:5120
	v_cvt_pk_bf16_f32 v0, v0, v1
	v_cvt_pk_bf16_f32 v1, v2, v3
	v_cvt_pk_bf16_f32 v2, v4, v5
	v_cvt_pk_bf16_f32 v3, v6, v7
	v_pk_max_i16 v0, v0, 0
	v_pk_max_i16 v1, v1, 0
	v_mfma_f32_32x32x16_bf16 v[80:95], v[116:119], v[100:103], v[80:95]
	v_pk_max_i16 v2, v2, 0
	v_pk_max_i16 v3, v3, 0
	ds_read_b128 v[4:7], v160 offset:7168
	v_cvt_pk_bf16_f32 v12, v12, v13
	v_cvt_pk_bf16_f32 v13, v14, v15
	v_cvt_pk_bf16_f32 v24, v24, v25
	v_cvt_pk_bf16_f32 v25, v26, v27
	s_waitcnt lgkmcnt(3)
	v_mfma_f32_32x32x16_bf16 v[64:79], v[144:147], v[104:107], v[64:79]
	v_cvt_pk_bf16_f32 v26, v28, v29
	v_cvt_pk_bf16_f32 v27, v30, v31
	v_cndmask_b32_e64 v219, v219, 0, s[14:15]
	v_cndmask_b32_e64 v218, v218, 0, s[14:15]
	v_mfma_f32_32x32x16_bf16 v[80:95], v[144:147], v[108:111], v[80:95]
	s_waitcnt lgkmcnt(2)
	v_mfma_f32_32x32x16_bf16 v[64:79], v[36:39], v[32:35], v[64:79]
	v_cvt_pk_bf16_f32 v34, v20, v21
	v_cvt_pk_bf16_f32 v35, v22, v23
	ds_read_b128 v[20:23], v160 offset:6144
	v_cvt_pk_bf16_f32 v32, v16, v17
	v_cvt_pk_bf16_f32 v33, v18, v19
	v_pk_max_i16 v16, v52, 0
	v_pk_max_i16 v17, v53, 0
	v_mfma_f32_32x32x16_bf16 v[80:95], v[36:39], v[48:51], v[80:95]
	v_pk_max_i16 v18, v54, 0
	v_pk_max_i16 v19, v55, 0
	s_waitcnt lgkmcnt(2)
	v_mfma_f32_32x32x16_bf16 v[64:79], v[96:99], v[40:43], v[64:79]
	v_mfma_f32_32x32x16_bf16 v[80:95], v[96:99], v[16:19], v[80:95]
	v_cvt_pk_bf16_f32 v16, v8, v9
	v_cvt_pk_bf16_f32 v17, v10, v11
	v_pk_max_i16 v8, v24, 0
	v_pk_max_i16 v9, v25, 0
	v_pk_max_i16 v10, v26, 0
	v_pk_max_i16 v11, v27, 0
	s_waitcnt lgkmcnt(0)
	v_mfma_f32_32x32x16_bf16 v[64:79], v[20:23], v[0:3], v[64:79]
	v_pk_max_i16 v0, v32, 0
	v_pk_max_i16 v1, v33, 0
	v_pk_max_i16 v2, v34, 0
	v_pk_max_i16 v3, v35, 0
	s_nop 1
	v_mfma_f32_32x32x16_bf16 v[80:95], v[20:23], v[0:3], v[80:95]
	v_pk_max_i16 v0, v16, 0
	v_pk_max_i16 v1, v17, 0
	v_pk_max_i16 v2, v12, 0
	v_pk_max_i16 v3, v13, 0
	s_nop 1
	v_mfma_f32_32x32x16_bf16 v[64:79], v[4:7], v[0:3], v[64:79]
	v_and_b32_e32 v1, 64, v229
	v_xor_b32_e32 v0, 32, v229
	v_add_u32_e32 v2, 64, v1
	v_cmp_lt_i32_e32 vcc, v0, v2
	s_nop 1
	v_cndmask_b32_e32 v0, v229, v0, vcc
	v_mfma_f32_32x32x16_bf16 v[80:95], v[4:7], v[8:11], v[80:95]
	v_lshlrev_b32_e32 v0, 2, v0
	s_waitcnt vmcnt(10)
	ds_bpermute_b32 v1, v0, v232
	s_and_saveexec_b64 s[14:15], s[0:1]
	s_cbranch_execz .LBB1_14
	v_add_f32_e32 v3, s10, v64
	v_mul_f32_e32 v3, 0xbfb8aa3b, v3
	v_exp_f32_e32 v4, v3
	v_add_f32_e32 v3, s11, v65
	v_mul_f32_e32 v3, 0xbfb8aa3b, v3
	v_exp_f32_e32 v5, v3
	s_nop 0
	v_add_f32_e32 v3, s10, v80
	v_mul_f32_e32 v3, 0xbfb8aa3b, v3
	v_exp_f32_e32 v6, v3
	v_pk_add_f32 v[4:5], v[4:5], 1.0 op_sel_hi:[1,0]
	v_add_f32_e32 v7, s11, v81
	v_div_scale_f32 v3, s[20:21], v5, v5, v232
	v_rcp_f32_e32 v8, v3
	v_mul_f32_e32 v7, 0xbfb8aa3b, v7
	v_exp_f32_e32 v7, v7
	v_fma_f32 v9, -v3, v8, 1.0
	v_fmac_f32_e32 v8, v9, v8
	v_div_scale_f32 v9, vcc, v232, v5, v232
	v_mul_f32_e32 v10, v9, v8
	v_fma_f32 v11, -v3, v10, v9
	v_fmac_f32_e32 v10, v11, v8
	v_fma_f32 v3, -v3, v10, v9
	v_div_scale_f32 v9, s[20:21], v4, v4, v232
	v_rcp_f32_e32 v11, v9
	v_div_fmas_f32 v3, v3, v8, v10
	v_div_fixup_f32 v5, v3, v5, v232
	v_pk_add_f32 v[6:7], v[6:7], 1.0 op_sel_hi:[1,0]
	v_fma_f32 v3, -v9, v11, 1.0
	v_fmac_f32_e32 v11, v3, v11
	v_div_scale_f32 v3, vcc, v232, v4, v232
	v_mul_f32_e32 v8, v3, v11
	v_fma_f32 v10, -v9, v8, v3
	v_fmac_f32_e32 v8, v10, v11
	v_fma_f32 v3, -v9, v8, v3
	s_waitcnt lgkmcnt(0)
	v_div_scale_f32 v9, s[20:21], v7, v7, v1
	v_rcp_f32_e32 v10, v9
	v_div_fmas_f32 v3, v3, v11, v8
	v_div_fixup_f32 v4, v3, v4, v232
	v_fma_f32 v3, -v9, v10, 1.0
	v_fmac_f32_e32 v10, v3, v10
	v_div_scale_f32 v3, vcc, v1, v7, v1
	v_mul_f32_e32 v8, v3, v10
	v_fma_f32 v11, -v9, v8, v3
	v_fmac_f32_e32 v8, v11, v10
	v_div_scale_f32 v11, s[20:21], v6, v6, v1
	v_rcp_f32_e32 v12, v11
	v_fma_f32 v3, -v9, v8, v3
	v_div_fmas_f32 v3, v3, v10, v8
	v_div_fixup_f32 v7, v3, v7, v1
	v_fma_f32 v3, -v11, v12, 1.0
	v_fmac_f32_e32 v12, v3, v12
	v_div_scale_f32 v3, vcc, v1, v6, v1
	v_mul_f32_e32 v10, v3, v12
	v_fma_f32 v8, -v11, v10, v3
	v_fmac_f32_e32 v10, v8, v12
	v_add_f32_e32 v8, s18, v66
	v_add_f32_e32 v9, s18, v82
	v_mul_f32_e32 v8, 0xbfb8aa3b, v8
	v_mul_f32_e32 v9, 0xbfb8aa3b, v9
	v_exp_f32_e32 v8, v8
	v_exp_f32_e32 v9, v9
	v_fma_f32 v3, -v11, v10, v3
	v_div_fmas_f32 v3, v3, v12, v10
	v_div_fixup_f32 v6, v3, v6, v1
	v_pk_add_f32 v[8:9], v[8:9], 1.0 op_sel_hi:[1,0]
	v_pk_add_f32 v[4:5], v[4:5], v[6:7]
	v_div_scale_f32 v10, s[20:21], v9, v9, v1
	v_rcp_f32_e32 v11, v10
	v_pk_add_f32 v[218:219], v[218:219], v[4:5]
	v_fma_f32 v3, -v10, v11, 1.0
	v_fmac_f32_e32 v11, v3, v11
	v_div_scale_f32 v3, vcc, v1, v9, v1
	v_mul_f32_e32 v4, v3, v11
	v_fma_f32 v5, -v10, v4, v3
	v_fmac_f32_e32 v4, v5, v11
	v_div_scale_f32 v5, s[20:21], v8, v8, v232
	v_rcp_f32_e32 v6, v5
	v_fma_f32 v3, -v10, v4, v3
	v_div_fmas_f32 v3, v3, v11, v4
	v_div_fixup_f32 v1, v3, v9, v1
	v_fma_f32 v3, -v5, v6, 1.0
	v_fmac_f32_e32 v6, v3, v6
	v_div_scale_f32 v3, vcc, v232, v8, v232
	v_mul_f32_e32 v4, v3, v6
	v_fma_f32 v7, -v5, v4, v3
	v_fmac_f32_e32 v4, v7, v6
	v_fma_f32 v3, -v5, v4, v3
	v_div_fmas_f32 v3, v3, v6, v4
	v_div_fixup_f32 v3, v3, v8, v232
	v_add_f32_e32 v1, v3, v1
	v_add_f32_e32 v230, v230, v1
